# E21: E19 + act re-quantisation loop software-pipelined (unrolled x2 with two register sets, next iteration's 6 loads issued before processing the current rows)
# baseline (speedup 1.0000x reference)
.LBB0_1291:
	s_or_b64 exec, exec, s[0:1]
	s_waitcnt lgkmcnt(0)
	v_mov_b32_e32 v1, v226
	v_mov_b32_e32 v11, 0
	s_barrier
	global_load_dword v0, v11, s[8:9]
	v_readfirstlane_b32 s0, v1
	s_ashr_i32 s0, s0, 6
	v_readlane_b32 s1, v252, 31
	s_add_i32 s6, s0, s1
	s_waitcnt vmcnt(0)
	v_readfirstlane_b32 s0, v0
	s_lshl_b32 s16, s0, 8
	v_readlane_b32 s0, v252, 2
	v_readlane_b32 s1, v252, 3
	s_add_u32 s10, s0, 0x207f8a00
	s_addc_u32 s11, s1, 0
	s_cmp_ge_i32 s6, s16
	s_cbranch_scc1 .LBB0_1300
	v_and_b32_e32 v0, 63, v1
	v_mbcnt_lo_u32_b32 v1, -1, 0
	v_mbcnt_hi_u32_b32 v2, -1, v1
	v_and_b32_e32 v1, 64, v2
	v_add_u32_e32 v3, 64, v1
	v_xor_b32_e32 v1, 1, v2
	v_cmp_lt_i32_e32 vcc, v1, v3
	v_xor_b32_e32 v4, 2, v2
	v_lshlrev_b32_e32 v10, 2, v0
	v_cndmask_b32_e32 v1, v2, v1, vcc
	v_cmp_lt_i32_e32 vcc, v4, v3
	v_lshl_add_u64 v[12:13], s[12:13], 0, v[10:11]
	v_lshlrev_b32_e32 v10, 5, v0
	v_cndmask_b32_e32 v4, v2, v4, vcc
	v_lshl_add_u64 v[14:15], s[2:3], 0, v[10:11]
	v_lshlrev_b32_e32 v10, 2, v4
	v_xor_b32_e32 v4, 4, v2
	v_cmp_lt_i32_e32 vcc, v4, v3
	v_lshlrev_b32_e32 v1, 2, v1
	v_cmp_eq_u32_e64 s[0:1], 0, v0
	v_cndmask_b32_e32 v4, v2, v4, vcc
	v_lshlrev_b32_e32 v18, 2, v4
	v_xor_b32_e32 v4, 8, v2
	v_cmp_lt_i32_e32 vcc, v4, v3
	s_mov_b32 s17, 0xc0c0400
	v_readlane_b32 s12, v252, 29
	v_cndmask_b32_e32 v4, v2, v4, vcc
	v_lshlrev_b32_e32 v19, 2, v4
	v_xor_b32_e32 v4, 16, v2
	v_cmp_lt_i32_e32 vcc, v4, v3
	v_readlane_b32 s13, v252, 30
	s_nop 0
	v_cndmask_b32_e32 v4, v2, v4, vcc
	v_lshlrev_b32_e32 v20, 2, v4
	v_xor_b32_e32 v4, 32, v2
	v_cmp_lt_i32_e32 vcc, v4, v3
	s_nop 1
	v_cndmask_b32_e32 v2, v2, v4, vcc
	v_lshlrev_b32_e32 v21, 2, v2
	v_readlane_b32 s60, v252, 29
	s_mov_b32 s61, s6
	s_add_i32 s62, s61, s60
	s_cmp_lt_i32 s62, s16
	s_cselect_b32 s62, s62, s61
	s_ashr_i32 s63, s62, 31
	s_mov_b32 s64, s61
	s_ashr_i32 s65, s61, 31
	s_lshl_b64 s[66:67], s[64:65], 8
	v_lshl_add_u64 v[82:83], v[12:13], 0, s[66:67]
	global_load_dword v0, v[82:83], off
	s_lshl_b64 s[66:67], s[64:65], 11
	v_lshl_add_u64 v[36:37], v[14:15], 0, s[66:67]
	s_lshl_b64 s[66:67], s[62:63], 8
	s_waitcnt lgkmcnt(0)
	global_load_dwordx4 v[24:27], v[36:37], off offset:16
	v_lshl_add_u64 v[82:83], v[12:13], 0, s[66:67]
	global_load_dword v22, v[82:83], off
	global_load_dwordx4 v[28:31], v[36:37], off
	s_lshl_b64 s[66:67], s[62:63], 11
	v_lshl_add_u64 v[16:17], v[14:15], 0, s[66:67]
	global_load_dwordx4 v[2:5], v[16:17], off offset:16
	global_load_dwordx4 v[6:9], v[16:17], off
.Lq_top_A:
	s_add_i32 s4, s6, s12
	s_cmp_lt_i32 s4, s16
	s_cselect_b64 s[12:13], -1, 0
	s_ashr_i32 s7, s6, 31
	v_readlane_b32 s60, v252, 29
	s_add_i32 s61, s4, s60
	s_cmp_lt_i32 s61, s16
	s_cselect_b32 s61, s61, s6
	s_add_i32 s62, s61, s60
	s_cmp_lt_i32 s62, s16
	s_cselect_b32 s62, s62, s61
	s_ashr_i32 s63, s62, 31
	s_mov_b32 s64, s61
	s_ashr_i32 s65, s61, 31
	s_lshl_b64 s[66:67], s[64:65], 8
	v_lshl_add_u64 v[82:83], v[12:13], 0, s[66:67]
	global_load_dword v60, v[82:83], off
	s_lshl_b64 s[66:67], s[64:65], 11
	v_lshl_add_u64 v[78:79], v[14:15], 0, s[66:67]
	s_lshl_b64 s[66:67], s[62:63], 8
	s_waitcnt lgkmcnt(0)
	global_load_dwordx4 v[62:65], v[78:79], off offset:16
	v_lshl_add_u64 v[82:83], v[12:13], 0, s[66:67]
	global_load_dword v61, v[82:83], off
	global_load_dwordx4 v[66:69], v[78:79], off
	s_lshl_b64 s[66:67], s[62:63], 11
	v_lshl_add_u64 v[80:81], v[14:15], 0, s[66:67]
	global_load_dwordx4 v[70:73], v[80:81], off offset:16
	global_load_dwordx4 v[74:77], v[80:81], off
	s_waitcnt vmcnt(6)
	ds_bpermute_b32 v23, v1, v0
	v_max_f32_e32 v32, v0, v0
	v_cvt_f32_i32_sdwa v33, sext(v24) dst_sel:DWORD dst_unused:UNUSED_PAD src0_sel:BYTE_0
	s_waitcnt lgkmcnt(0)
	v_max_f32_e32 v23, v23, v23
	v_max_f32_e32 v23, v32, v23
	ds_bpermute_b32 v32, v10, v23
	v_cvt_f32_i32_sdwa v34, sext(v24) dst_sel:DWORD dst_unused:UNUSED_PAD src0_sel:BYTE_1
	v_cvt_f32_i32_sdwa v35, sext(v24) dst_sel:DWORD dst_unused:UNUSED_PAD src0_sel:BYTE_2
	v_cvt_f32_i32_sdwa v38, sext(v24) dst_sel:DWORD dst_unused:UNUSED_PAD src0_sel:BYTE_3
	ds_bpermute_b32 v24, v1, v22
	s_waitcnt lgkmcnt(1)
	v_max_f32_e32 v32, v32, v32
	v_max_f32_e32 v23, v23, v32
	ds_bpermute_b32 v32, v18, v23
	v_cvt_f32_i32_sdwa v39, sext(v25) dst_sel:DWORD dst_unused:UNUSED_PAD src0_sel:BYTE_0
	v_cvt_f32_i32_sdwa v40, sext(v25) dst_sel:DWORD dst_unused:UNUSED_PAD src0_sel:BYTE_1
	v_cvt_f32_i32_sdwa v41, sext(v25) dst_sel:DWORD dst_unused:UNUSED_PAD src0_sel:BYTE_2
	v_cvt_f32_i32_sdwa v42, sext(v25) dst_sel:DWORD dst_unused:UNUSED_PAD src0_sel:BYTE_3
	v_max_f32_e32 v25, v22, v22
	s_waitcnt lgkmcnt(1)
	v_max_f32_e32 v24, v24, v24
	v_max_f32_e32 v24, v25, v24
	s_waitcnt lgkmcnt(0)
	v_max_f32_e32 v32, v32, v32
	ds_bpermute_b32 v25, v10, v24
	v_max_f32_e32 v23, v23, v32
	ds_bpermute_b32 v32, v19, v23
	v_cvt_f32_i32_sdwa v43, sext(v26) dst_sel:DWORD dst_unused:UNUSED_PAD src0_sel:BYTE_0
	v_cvt_f32_i32_sdwa v44, sext(v26) dst_sel:DWORD dst_unused:UNUSED_PAD src0_sel:BYTE_1
	s_waitcnt lgkmcnt(1)
	v_max_f32_e32 v25, v25, v25
	v_max_f32_e32 v24, v24, v25
	s_waitcnt lgkmcnt(0)
	v_max_f32_e32 v32, v32, v32
	ds_bpermute_b32 v25, v18, v24
	v_max_f32_e32 v23, v23, v32
	ds_bpermute_b32 v32, v20, v23
	v_cvt_f32_i32_sdwa v45, sext(v26) dst_sel:DWORD dst_unused:UNUSED_PAD src0_sel:BYTE_2
	v_cvt_f32_i32_sdwa v26, sext(v26) dst_sel:DWORD dst_unused:UNUSED_PAD src0_sel:BYTE_3
	s_waitcnt lgkmcnt(1)
	v_max_f32_e32 v25, v25, v25
	v_max_f32_e32 v24, v24, v25
	s_waitcnt lgkmcnt(0)
	v_max_f32_e32 v32, v32, v32
	ds_bpermute_b32 v25, v19, v24
	v_max_f32_e32 v23, v23, v32
	ds_bpermute_b32 v32, v21, v23
	v_cvt_f32_i32_sdwa v46, sext(v28) dst_sel:DWORD dst_unused:UNUSED_PAD src0_sel:BYTE_0
	v_cvt_f32_i32_sdwa v47, sext(v28) dst_sel:DWORD dst_unused:UNUSED_PAD src0_sel:BYTE_1
	s_waitcnt lgkmcnt(1)
	v_max_f32_e32 v25, v25, v25
	v_max_f32_e32 v24, v24, v25
	s_waitcnt lgkmcnt(0)
	v_max_f32_e32 v25, v32, v32
	v_max_f32_e32 v25, v23, v25
	v_rcp_f32_e32 v32, v25
	v_cvt_f32_i32_sdwa v48, sext(v28) dst_sel:DWORD dst_unused:UNUSED_PAD src0_sel:BYTE_2
	v_cvt_f32_i32_sdwa v28, sext(v28) dst_sel:DWORD dst_unused:UNUSED_PAD src0_sel:BYTE_3
	ds_bpermute_b32 v58, v20, v24
	v_mul_f32_e32 v0, v0, v32
	v_cmp_lt_f32_e32 vcc, 0, v25
	v_cvt_f32_i32_sdwa v49, sext(v29) dst_sel:DWORD dst_unused:UNUSED_PAD src0_sel:BYTE_0
	v_cvt_f32_i32_sdwa v50, sext(v29) dst_sel:DWORD dst_unused:UNUSED_PAD src0_sel:BYTE_1
	v_cndmask_b32_e32 v0, 0, v0, vcc
	v_fmaak_f32 v32, v0, v46, 0x4b400000
	v_fmaak_f32 v46, v0, v47, 0x4b400000
	v_fmaak_f32 v47, v0, v48, 0x4b400000
	v_fmaak_f32 v28, v0, v28, 0x4b400000
	v_fmaak_f32 v33, v0, v33, 0x4b400000
	v_fmaak_f32 v34, v0, v34, 0x4b400000
	v_fmaak_f32 v35, v0, v35, 0x4b400000
	v_fmaak_f32 v38, v0, v38, 0x4b400000
	v_fmaak_f32 v39, v0, v39, 0x4b400000
	v_fmaak_f32 v40, v0, v40, 0x4b400000
	v_fmaak_f32 v41, v0, v41, 0x4b400000
	v_fmaak_f32 v42, v0, v42, 0x4b400000
	v_fmaak_f32 v43, v0, v43, 0x4b400000
	v_fmaak_f32 v44, v0, v44, 0x4b400000
	v_fmaak_f32 v45, v0, v45, 0x4b400000
	v_fmaak_f32 v26, v0, v26, 0x4b400000
	v_cvt_f32_i32_sdwa v51, sext(v29) dst_sel:DWORD dst_unused:UNUSED_PAD src0_sel:BYTE_2
	v_cvt_f32_i32_sdwa v29, sext(v29) dst_sel:DWORD dst_unused:UNUSED_PAD src0_sel:BYTE_3
	v_cvt_f32_i32_sdwa v52, sext(v30) dst_sel:DWORD dst_unused:UNUSED_PAD src0_sel:BYTE_0
	v_cvt_f32_i32_sdwa v53, sext(v30) dst_sel:DWORD dst_unused:UNUSED_PAD src0_sel:BYTE_1
	v_cvt_f32_i32_sdwa v54, sext(v30) dst_sel:DWORD dst_unused:UNUSED_PAD src0_sel:BYTE_2
	v_cvt_f32_i32_sdwa v30, sext(v30) dst_sel:DWORD dst_unused:UNUSED_PAD src0_sel:BYTE_3
	v_cvt_f32_i32_sdwa v55, sext(v31) dst_sel:DWORD dst_unused:UNUSED_PAD src0_sel:BYTE_0
	v_cvt_f32_i32_sdwa v56, sext(v31) dst_sel:DWORD dst_unused:UNUSED_PAD src0_sel:BYTE_1
	v_cvt_f32_i32_sdwa v57, sext(v31) dst_sel:DWORD dst_unused:UNUSED_PAD src0_sel:BYTE_2
	v_cvt_f32_i32_sdwa v31, sext(v31) dst_sel:DWORD dst_unused:UNUSED_PAD src0_sel:BYTE_3
	s_waitcnt lgkmcnt(0)
	v_max_f32_e32 v23, v58, v58
	v_perm_b32 v32, v46, v32, s17
	v_perm_b32 v28, v28, v47, s17
	v_perm_b32 v33, v34, v33, s17
	v_perm_b32 v34, v38, v35, s17
	v_perm_b32 v35, v40, v39, s17
	v_perm_b32 v38, v42, v41, s17
	v_perm_b32 v39, v44, v43, s17
	v_perm_b32 v26, v26, v45, s17
	v_max_f32_e32 v23, v24, v23
	v_lshl_or_b32 v28, v28, 16, v32
	v_lshl_or_b32 v32, v34, 16, v33
	v_lshl_or_b32 v33, v38, 16, v35
	v_lshl_or_b32 v34, v26, 16, v39
	v_cvt_f32_i32_sdwa v26, sext(v27) dst_sel:DWORD dst_unused:UNUSED_PAD src0_sel:BYTE_0
	v_cvt_f32_i32_sdwa v35, sext(v27) dst_sel:DWORD dst_unused:UNUSED_PAD src0_sel:BYTE_1
	v_cvt_f32_i32_sdwa v38, sext(v27) dst_sel:DWORD dst_unused:UNUSED_PAD src0_sel:BYTE_2
	v_cvt_f32_i32_sdwa v27, sext(v27) dst_sel:DWORD dst_unused:UNUSED_PAD src0_sel:BYTE_3
	ds_bpermute_b32 v24, v21, v23
	v_fmaak_f32 v48, v0, v49, 0x4b400000
	v_fmaak_f32 v49, v0, v50, 0x4b400000
	v_fmaak_f32 v50, v0, v51, 0x4b400000
	v_fmaak_f32 v29, v0, v29, 0x4b400000
	v_fmaak_f32 v51, v0, v52, 0x4b400000
	v_fmaak_f32 v52, v0, v53, 0x4b400000
	v_fmaak_f32 v53, v0, v54, 0x4b400000
	v_fmaak_f32 v30, v0, v30, 0x4b400000
	v_fmaak_f32 v54, v0, v55, 0x4b400000
	v_fmaak_f32 v55, v0, v56, 0x4b400000
	v_fmaak_f32 v56, v0, v57, 0x4b400000
	v_fmaak_f32 v31, v0, v31, 0x4b400000
	v_perm_b32 v46, v49, v48, s17
	v_perm_b32 v29, v29, v50, s17
	v_perm_b32 v47, v52, v51, s17
	v_perm_b32 v30, v30, v53, s17
	v_perm_b32 v48, v55, v54, s17
	v_perm_b32 v31, v31, v56, s17
	v_fmaak_f32 v26, v0, v26, 0x4b400000
	v_fmaak_f32 v35, v0, v35, 0x4b400000
	v_fmaak_f32 v38, v0, v38, 0x4b400000
	v_fmaak_f32 v0, v0, v27, 0x4b400000
	v_lshl_or_b32 v29, v29, 16, v46
	v_lshl_or_b32 v30, v30, 16, v47
	v_lshl_or_b32 v31, v31, 16, v48
	v_perm_b32 v26, v35, v26, s17
	v_perm_b32 v0, v0, v38, s17
	v_lshl_or_b32 v35, v0, 16, v26
	global_store_dwordx4 v[36:37], v[28:31], off
	global_store_dwordx4 v[36:37], v[32:35], off offset:16
	s_and_saveexec_b64 s[14:15], s[0:1]
	s_cbranch_execz .Lq1297_A
	s_lshl_b64 s[6:7], s[6:7], 2
	v_mul_f32_e32 v0, 0x3c010204, v25
	s_add_u32 s6, s10, s6
	v_cndmask_b32_e32 v0, 1.0, v0, vcc
	s_addc_u32 s7, s11, s7
	global_store_dword v11, v0, s[6:7]
.Lq1297_A:
	s_or_b64 exec, exec, s[14:15]
	s_andn2_b64 vcc, exec, s[12:13]
	s_cbranch_vccnz .Lq1294_A
	s_waitcnt lgkmcnt(0)
	v_max_f32_e32 v0, v24, v24
	v_max_f32_e32 v23, v23, v23
	v_max_f32_e32 v23, v23, v0
	v_rcp_f32_e32 v0, v23
	v_cvt_f32_i32_sdwa v24, sext(v6) dst_sel:DWORD dst_unused:UNUSED_PAD src0_sel:BYTE_0
	v_cvt_f32_i32_sdwa v25, sext(v6) dst_sel:DWORD dst_unused:UNUSED_PAD src0_sel:BYTE_2
	v_cmp_lt_f32_e32 vcc, 0, v23
	v_mul_f32_e32 v0, v22, v0
	v_cvt_f32_i32_sdwa v22, sext(v6) dst_sel:DWORD dst_unused:UNUSED_PAD src0_sel:BYTE_1
	v_cvt_f32_i32_sdwa v6, sext(v6) dst_sel:DWORD dst_unused:UNUSED_PAD src0_sel:BYTE_3
	v_cndmask_b32_e32 v0, 0, v0, vcc
	v_fmaak_f32 v24, v0, v24, 0x4b400000
	v_fmaak_f32 v22, v0, v22, 0x4b400000
	v_fmaak_f32 v25, v0, v25, 0x4b400000
	v_fmaak_f32 v6, v0, v6, 0x4b400000
	v_perm_b32 v22, v22, v24, s17
	v_perm_b32 v6, v6, v25, s17
	v_lshl_or_b32 v6, v6, 16, v22
	v_cvt_f32_i32_sdwa v22, sext(v7) dst_sel:DWORD dst_unused:UNUSED_PAD src0_sel:BYTE_0
	v_cvt_f32_i32_sdwa v24, sext(v7) dst_sel:DWORD dst_unused:UNUSED_PAD src0_sel:BYTE_1
	v_cvt_f32_i32_sdwa v25, sext(v7) dst_sel:DWORD dst_unused:UNUSED_PAD src0_sel:BYTE_2
	v_cvt_f32_i32_sdwa v7, sext(v7) dst_sel:DWORD dst_unused:UNUSED_PAD src0_sel:BYTE_3
	v_fmaak_f32 v22, v0, v22, 0x4b400000
	v_fmaak_f32 v24, v0, v24, 0x4b400000
	v_fmaak_f32 v25, v0, v25, 0x4b400000
	v_fmaak_f32 v7, v0, v7, 0x4b400000
	v_perm_b32 v22, v24, v22, s17
	v_perm_b32 v7, v7, v25, s17
	v_lshl_or_b32 v7, v7, 16, v22
	v_cvt_f32_i32_sdwa v22, sext(v8) dst_sel:DWORD dst_unused:UNUSED_PAD src0_sel:BYTE_0
	v_cvt_f32_i32_sdwa v24, sext(v8) dst_sel:DWORD dst_unused:UNUSED_PAD src0_sel:BYTE_1
	v_cvt_f32_i32_sdwa v25, sext(v8) dst_sel:DWORD dst_unused:UNUSED_PAD src0_sel:BYTE_2
	v_cvt_f32_i32_sdwa v8, sext(v8) dst_sel:DWORD dst_unused:UNUSED_PAD src0_sel:BYTE_3
	v_fmaak_f32 v22, v0, v22, 0x4b400000
	v_fmaak_f32 v24, v0, v24, 0x4b400000
	v_fmaak_f32 v25, v0, v25, 0x4b400000
	v_fmaak_f32 v8, v0, v8, 0x4b400000
	v_perm_b32 v22, v24, v22, s17
	v_perm_b32 v8, v8, v25, s17
	v_lshl_or_b32 v8, v8, 16, v22
	v_cvt_f32_i32_sdwa v22, sext(v9) dst_sel:DWORD dst_unused:UNUSED_PAD src0_sel:BYTE_0
	v_cvt_f32_i32_sdwa v24, sext(v9) dst_sel:DWORD dst_unused:UNUSED_PAD src0_sel:BYTE_1
	v_cvt_f32_i32_sdwa v25, sext(v9) dst_sel:DWORD dst_unused:UNUSED_PAD src0_sel:BYTE_2
	v_cvt_f32_i32_sdwa v9, sext(v9) dst_sel:DWORD dst_unused:UNUSED_PAD src0_sel:BYTE_3
	v_fmaak_f32 v22, v0, v22, 0x4b400000
	v_fmaak_f32 v24, v0, v24, 0x4b400000
	v_fmaak_f32 v25, v0, v25, 0x4b400000
	v_fmaak_f32 v9, v0, v9, 0x4b400000
	v_perm_b32 v22, v24, v22, s17
	v_perm_b32 v9, v9, v25, s17
	v_lshl_or_b32 v9, v9, 16, v22
	v_cvt_f32_i32_sdwa v22, sext(v2) dst_sel:DWORD dst_unused:UNUSED_PAD src0_sel:BYTE_0
	v_cvt_f32_i32_sdwa v24, sext(v2) dst_sel:DWORD dst_unused:UNUSED_PAD src0_sel:BYTE_1
	v_cvt_f32_i32_sdwa v25, sext(v2) dst_sel:DWORD dst_unused:UNUSED_PAD src0_sel:BYTE_2
	v_cvt_f32_i32_sdwa v2, sext(v2) dst_sel:DWORD dst_unused:UNUSED_PAD src0_sel:BYTE_3
	v_fmaak_f32 v22, v0, v22, 0x4b400000
	v_fmaak_f32 v24, v0, v24, 0x4b400000
	v_fmaak_f32 v25, v0, v25, 0x4b400000
	v_fmaak_f32 v2, v0, v2, 0x4b400000
	v_perm_b32 v22, v24, v22, s17
	v_perm_b32 v2, v2, v25, s17
	v_lshl_or_b32 v2, v2, 16, v22
	v_cvt_f32_i32_sdwa v22, sext(v3) dst_sel:DWORD dst_unused:UNUSED_PAD src0_sel:BYTE_0
	v_cvt_f32_i32_sdwa v24, sext(v3) dst_sel:DWORD dst_unused:UNUSED_PAD src0_sel:BYTE_1
	v_cvt_f32_i32_sdwa v25, sext(v3) dst_sel:DWORD dst_unused:UNUSED_PAD src0_sel:BYTE_2
	v_cvt_f32_i32_sdwa v3, sext(v3) dst_sel:DWORD dst_unused:UNUSED_PAD src0_sel:BYTE_3
	v_fmaak_f32 v22, v0, v22, 0x4b400000
	v_fmaak_f32 v24, v0, v24, 0x4b400000
	v_fmaak_f32 v25, v0, v25, 0x4b400000
	v_fmaak_f32 v3, v0, v3, 0x4b400000
	v_perm_b32 v22, v24, v22, s17
	v_perm_b32 v3, v3, v25, s17
	v_lshl_or_b32 v3, v3, 16, v22
	v_cvt_f32_i32_sdwa v22, sext(v4) dst_sel:DWORD dst_unused:UNUSED_PAD src0_sel:BYTE_0
	v_cvt_f32_i32_sdwa v24, sext(v4) dst_sel:DWORD dst_unused:UNUSED_PAD src0_sel:BYTE_1
	v_cvt_f32_i32_sdwa v25, sext(v4) dst_sel:DWORD dst_unused:UNUSED_PAD src0_sel:BYTE_2
	v_cvt_f32_i32_sdwa v4, sext(v4) dst_sel:DWORD dst_unused:UNUSED_PAD src0_sel:BYTE_3
	v_fmaak_f32 v22, v0, v22, 0x4b400000
	v_fmaak_f32 v24, v0, v24, 0x4b400000
	v_fmaak_f32 v25, v0, v25, 0x4b400000
	v_fmaak_f32 v4, v0, v4, 0x4b400000
	v_perm_b32 v22, v24, v22, s17
	v_perm_b32 v4, v4, v25, s17
	v_lshl_or_b32 v4, v4, 16, v22
	v_cvt_f32_i32_sdwa v22, sext(v5) dst_sel:DWORD dst_unused:UNUSED_PAD src0_sel:BYTE_0
	v_cvt_f32_i32_sdwa v24, sext(v5) dst_sel:DWORD dst_unused:UNUSED_PAD src0_sel:BYTE_1
	v_cvt_f32_i32_sdwa v25, sext(v5) dst_sel:DWORD dst_unused:UNUSED_PAD src0_sel:BYTE_2
	v_cvt_f32_i32_sdwa v5, sext(v5) dst_sel:DWORD dst_unused:UNUSED_PAD src0_sel:BYTE_3
	v_fmaak_f32 v22, v0, v22, 0x4b400000
	v_fmaak_f32 v24, v0, v24, 0x4b400000
	v_fmaak_f32 v25, v0, v25, 0x4b400000
	v_fmaak_f32 v0, v0, v5, 0x4b400000
	v_perm_b32 v5, v24, v22, s17
	v_perm_b32 v0, v0, v25, s17
	v_lshl_or_b32 v5, v0, 16, v5
	global_store_dwordx4 v[16:17], v[6:9], off
	global_store_dwordx4 v[16:17], v[2:5], off offset:16
	s_and_saveexec_b64 s[6:7], s[0:1]
	s_cbranch_execz .Lq1293_A
	s_ashr_i32 s5, s4, 31
	s_lshl_b64 s[12:13], s[4:5], 2
	v_mul_f32_e32 v0, 0x3c010204, v23
	s_add_u32 s12, s10, s12
	v_cndmask_b32_e32 v0, 1.0, v0, vcc
	s_addc_u32 s13, s11, s13
	global_store_dword v11, v0, s[12:13]

.Lq_top_B:
	s_add_i32 s4, s6, s12
	s_cmp_lt_i32 s4, s16
	s_cselect_b64 s[12:13], -1, 0
	s_ashr_i32 s7, s6, 31
	v_readlane_b32 s60, v252, 29
	s_add_i32 s61, s4, s60
	s_cmp_lt_i32 s61, s16
	s_cselect_b32 s61, s61, s6
	s_add_i32 s62, s61, s60
	s_cmp_lt_i32 s62, s16
	s_cselect_b32 s62, s62, s61
	s_ashr_i32 s63, s62, 31
	s_mov_b32 s64, s61
	s_ashr_i32 s65, s61, 31
	s_lshl_b64 s[66:67], s[64:65], 8
	v_lshl_add_u64 v[82:83], v[12:13], 0, s[66:67]
	global_load_dword v0, v[82:83], off
	s_lshl_b64 s[66:67], s[64:65], 11
	v_lshl_add_u64 v[36:37], v[14:15], 0, s[66:67]
	s_lshl_b64 s[66:67], s[62:63], 8
	s_waitcnt lgkmcnt(0)
	global_load_dwordx4 v[24:27], v[36:37], off offset:16
	v_lshl_add_u64 v[82:83], v[12:13], 0, s[66:67]
	global_load_dword v22, v[82:83], off
	global_load_dwordx4 v[28:31], v[36:37], off
	s_lshl_b64 s[66:67], s[62:63], 11
	v_lshl_add_u64 v[16:17], v[14:15], 0, s[66:67]
	global_load_dwordx4 v[2:5], v[16:17], off offset:16
	global_load_dwordx4 v[6:9], v[16:17], off
	s_waitcnt vmcnt(6)
	ds_bpermute_b32 v23, v1, v60
	v_max_f32_e32 v32, v60, v60
	v_cvt_f32_i32_sdwa v33, sext(v62) dst_sel:DWORD dst_unused:UNUSED_PAD src0_sel:BYTE_0
	s_waitcnt lgkmcnt(0)
	v_max_f32_e32 v23, v23, v23
	v_max_f32_e32 v23, v32, v23
	ds_bpermute_b32 v32, v10, v23
	v_cvt_f32_i32_sdwa v34, sext(v62) dst_sel:DWORD dst_unused:UNUSED_PAD src0_sel:BYTE_1
	v_cvt_f32_i32_sdwa v35, sext(v62) dst_sel:DWORD dst_unused:UNUSED_PAD src0_sel:BYTE_2
	v_cvt_f32_i32_sdwa v38, sext(v62) dst_sel:DWORD dst_unused:UNUSED_PAD src0_sel:BYTE_3
	ds_bpermute_b32 v62, v1, v61
	s_waitcnt lgkmcnt(1)
	v_max_f32_e32 v32, v32, v32
	v_max_f32_e32 v23, v23, v32
	ds_bpermute_b32 v32, v18, v23
	v_cvt_f32_i32_sdwa v39, sext(v63) dst_sel:DWORD dst_unused:UNUSED_PAD src0_sel:BYTE_0
	v_cvt_f32_i32_sdwa v40, sext(v63) dst_sel:DWORD dst_unused:UNUSED_PAD src0_sel:BYTE_1
	v_cvt_f32_i32_sdwa v41, sext(v63) dst_sel:DWORD dst_unused:UNUSED_PAD src0_sel:BYTE_2
	v_cvt_f32_i32_sdwa v42, sext(v63) dst_sel:DWORD dst_unused:UNUSED_PAD src0_sel:BYTE_3
	v_max_f32_e32 v63, v61, v61
	s_waitcnt lgkmcnt(1)
	v_max_f32_e32 v62, v62, v62
	v_max_f32_e32 v62, v63, v62
	s_waitcnt lgkmcnt(0)
	v_max_f32_e32 v32, v32, v32
	ds_bpermute_b32 v63, v10, v62
	v_max_f32_e32 v23, v23, v32
	ds_bpermute_b32 v32, v19, v23
	v_cvt_f32_i32_sdwa v43, sext(v64) dst_sel:DWORD dst_unused:UNUSED_PAD src0_sel:BYTE_0
	v_cvt_f32_i32_sdwa v44, sext(v64) dst_sel:DWORD dst_unused:UNUSED_PAD src0_sel:BYTE_1
	s_waitcnt lgkmcnt(1)
	v_max_f32_e32 v63, v63, v63
	v_max_f32_e32 v62, v62, v63
	s_waitcnt lgkmcnt(0)
	v_max_f32_e32 v32, v32, v32
	ds_bpermute_b32 v63, v18, v62
	v_max_f32_e32 v23, v23, v32
	ds_bpermute_b32 v32, v20, v23
	v_cvt_f32_i32_sdwa v45, sext(v64) dst_sel:DWORD dst_unused:UNUSED_PAD src0_sel:BYTE_2
	v_cvt_f32_i32_sdwa v64, sext(v64) dst_sel:DWORD dst_unused:UNUSED_PAD src0_sel:BYTE_3
	s_waitcnt lgkmcnt(1)
	v_max_f32_e32 v63, v63, v63
	v_max_f32_e32 v62, v62, v63
	s_waitcnt lgkmcnt(0)
	v_max_f32_e32 v32, v32, v32
	ds_bpermute_b32 v63, v19, v62
	v_max_f32_e32 v23, v23, v32
	ds_bpermute_b32 v32, v21, v23
	v_cvt_f32_i32_sdwa v46, sext(v66) dst_sel:DWORD dst_unused:UNUSED_PAD src0_sel:BYTE_0
	v_cvt_f32_i32_sdwa v47, sext(v66) dst_sel:DWORD dst_unused:UNUSED_PAD src0_sel:BYTE_1
	s_waitcnt lgkmcnt(1)
	v_max_f32_e32 v63, v63, v63
	v_max_f32_e32 v62, v62, v63
	s_waitcnt lgkmcnt(0)
	v_max_f32_e32 v63, v32, v32
	v_max_f32_e32 v63, v23, v63
	v_rcp_f32_e32 v32, v63
	v_cvt_f32_i32_sdwa v48, sext(v66) dst_sel:DWORD dst_unused:UNUSED_PAD src0_sel:BYTE_2
	v_cvt_f32_i32_sdwa v66, sext(v66) dst_sel:DWORD dst_unused:UNUSED_PAD src0_sel:BYTE_3
	ds_bpermute_b32 v58, v20, v62
	v_mul_f32_e32 v60, v60, v32
	v_cmp_lt_f32_e32 vcc, 0, v63
	v_cvt_f32_i32_sdwa v49, sext(v67) dst_sel:DWORD dst_unused:UNUSED_PAD src0_sel:BYTE_0
	v_cvt_f32_i32_sdwa v50, sext(v67) dst_sel:DWORD dst_unused:UNUSED_PAD src0_sel:BYTE_1
	v_cndmask_b32_e32 v60, 0, v60, vcc
	v_fmaak_f32 v32, v60, v46, 0x4b400000
	v_fmaak_f32 v46, v60, v47, 0x4b400000
	v_fmaak_f32 v47, v60, v48, 0x4b400000
	v_fmaak_f32 v66, v60, v66, 0x4b400000
	v_fmaak_f32 v33, v60, v33, 0x4b400000
	v_fmaak_f32 v34, v60, v34, 0x4b400000
	v_fmaak_f32 v35, v60, v35, 0x4b400000
	v_fmaak_f32 v38, v60, v38, 0x4b400000
	v_fmaak_f32 v39, v60, v39, 0x4b400000
	v_fmaak_f32 v40, v60, v40, 0x4b400000
	v_fmaak_f32 v41, v60, v41, 0x4b400000
	v_fmaak_f32 v42, v60, v42, 0x4b400000
	v_fmaak_f32 v43, v60, v43, 0x4b400000
	v_fmaak_f32 v44, v60, v44, 0x4b400000
	v_fmaak_f32 v45, v60, v45, 0x4b400000
	v_fmaak_f32 v64, v60, v64, 0x4b400000
	v_cvt_f32_i32_sdwa v51, sext(v67) dst_sel:DWORD dst_unused:UNUSED_PAD src0_sel:BYTE_2
	v_cvt_f32_i32_sdwa v67, sext(v67) dst_sel:DWORD dst_unused:UNUSED_PAD src0_sel:BYTE_3
	v_cvt_f32_i32_sdwa v52, sext(v68) dst_sel:DWORD dst_unused:UNUSED_PAD src0_sel:BYTE_0
	v_cvt_f32_i32_sdwa v53, sext(v68) dst_sel:DWORD dst_unused:UNUSED_PAD src0_sel:BYTE_1
	v_cvt_f32_i32_sdwa v54, sext(v68) dst_sel:DWORD dst_unused:UNUSED_PAD src0_sel:BYTE_2
	v_cvt_f32_i32_sdwa v68, sext(v68) dst_sel:DWORD dst_unused:UNUSED_PAD src0_sel:BYTE_3
	v_cvt_f32_i32_sdwa v55, sext(v69) dst_sel:DWORD dst_unused:UNUSED_PAD src0_sel:BYTE_0
	v_cvt_f32_i32_sdwa v56, sext(v69) dst_sel:DWORD dst_unused:UNUSED_PAD src0_sel:BYTE_1
	v_cvt_f32_i32_sdwa v57, sext(v69) dst_sel:DWORD dst_unused:UNUSED_PAD src0_sel:BYTE_2
	v_cvt_f32_i32_sdwa v69, sext(v69) dst_sel:DWORD dst_unused:UNUSED_PAD src0_sel:BYTE_3
	s_waitcnt lgkmcnt(0)
	v_max_f32_e32 v23, v58, v58
	v_perm_b32 v32, v46, v32, s17
	v_perm_b32 v66, v66, v47, s17
	v_perm_b32 v33, v34, v33, s17
	v_perm_b32 v34, v38, v35, s17
	v_perm_b32 v35, v40, v39, s17
	v_perm_b32 v38, v42, v41, s17
	v_perm_b32 v39, v44, v43, s17
	v_perm_b32 v64, v64, v45, s17
	v_max_f32_e32 v23, v62, v23
	v_lshl_or_b32 v66, v66, 16, v32
	v_lshl_or_b32 v32, v34, 16, v33
	v_lshl_or_b32 v33, v38, 16, v35
	v_lshl_or_b32 v34, v64, 16, v39
	v_cvt_f32_i32_sdwa v64, sext(v65) dst_sel:DWORD dst_unused:UNUSED_PAD src0_sel:BYTE_0
	v_cvt_f32_i32_sdwa v35, sext(v65) dst_sel:DWORD dst_unused:UNUSED_PAD src0_sel:BYTE_1
	v_cvt_f32_i32_sdwa v38, sext(v65) dst_sel:DWORD dst_unused:UNUSED_PAD src0_sel:BYTE_2
	v_cvt_f32_i32_sdwa v65, sext(v65) dst_sel:DWORD dst_unused:UNUSED_PAD src0_sel:BYTE_3
	ds_bpermute_b32 v62, v21, v23
	v_fmaak_f32 v48, v60, v49, 0x4b400000
	v_fmaak_f32 v49, v60, v50, 0x4b400000
	v_fmaak_f32 v50, v60, v51, 0x4b400000
	v_fmaak_f32 v67, v60, v67, 0x4b400000
	v_fmaak_f32 v51, v60, v52, 0x4b400000
	v_fmaak_f32 v52, v60, v53, 0x4b400000
	v_fmaak_f32 v53, v60, v54, 0x4b400000
	v_fmaak_f32 v68, v60, v68, 0x4b400000
	v_fmaak_f32 v54, v60, v55, 0x4b400000
	v_fmaak_f32 v55, v60, v56, 0x4b400000
	v_fmaak_f32 v56, v60, v57, 0x4b400000
	v_fmaak_f32 v69, v60, v69, 0x4b400000
	v_perm_b32 v46, v49, v48, s17
	v_perm_b32 v67, v67, v50, s17
	v_perm_b32 v47, v52, v51, s17
	v_perm_b32 v68, v68, v53, s17
	v_perm_b32 v48, v55, v54, s17
	v_perm_b32 v69, v69, v56, s17
	v_fmaak_f32 v64, v60, v64, 0x4b400000
	v_fmaak_f32 v35, v60, v35, 0x4b400000
	v_fmaak_f32 v38, v60, v38, 0x4b400000
	v_fmaak_f32 v60, v60, v65, 0x4b400000
	v_lshl_or_b32 v67, v67, 16, v46
	v_lshl_or_b32 v68, v68, 16, v47
	v_lshl_or_b32 v69, v69, 16, v48
	v_perm_b32 v64, v35, v64, s17
	v_perm_b32 v60, v60, v38, s17
	v_lshl_or_b32 v35, v60, 16, v64
	global_store_dwordx4 v[78:79], v[66:69], off
	global_store_dwordx4 v[78:79], v[32:35], off offset:16
	s_and_saveexec_b64 s[14:15], s[0:1]
	s_cbranch_execz .Lq1297_B
	s_lshl_b64 s[6:7], s[6:7], 2
	v_mul_f32_e32 v60, 0x3c010204, v63
	s_add_u32 s6, s10, s6
	v_cndmask_b32_e32 v60, 1.0, v60, vcc
	s_addc_u32 s7, s11, s7
	global_store_dword v11, v60, s[6:7]
.Lq1297_B:
	s_or_b64 exec, exec, s[14:15]
	s_andn2_b64 vcc, exec, s[12:13]
	s_cbranch_vccnz .Lq1294_B
	s_waitcnt lgkmcnt(0)
	v_max_f32_e32 v60, v62, v62
	v_max_f32_e32 v23, v23, v23
	v_max_f32_e32 v23, v23, v60
	v_rcp_f32_e32 v60, v23
	v_cvt_f32_i32_sdwa v62, sext(v74) dst_sel:DWORD dst_unused:UNUSED_PAD src0_sel:BYTE_0
	v_cvt_f32_i32_sdwa v63, sext(v74) dst_sel:DWORD dst_unused:UNUSED_PAD src0_sel:BYTE_2
	v_cmp_lt_f32_e32 vcc, 0, v23
	v_mul_f32_e32 v60, v61, v60
	v_cvt_f32_i32_sdwa v61, sext(v74) dst_sel:DWORD dst_unused:UNUSED_PAD src0_sel:BYTE_1
	v_cvt_f32_i32_sdwa v74, sext(v74) dst_sel:DWORD dst_unused:UNUSED_PAD src0_sel:BYTE_3
	v_cndmask_b32_e32 v60, 0, v60, vcc
	v_fmaak_f32 v62, v60, v62, 0x4b400000
	v_fmaak_f32 v61, v60, v61, 0x4b400000
	v_fmaak_f32 v63, v60, v63, 0x4b400000
	v_fmaak_f32 v74, v60, v74, 0x4b400000
	v_perm_b32 v61, v61, v62, s17
	v_perm_b32 v74, v74, v63, s17
	v_lshl_or_b32 v74, v74, 16, v61
	v_cvt_f32_i32_sdwa v61, sext(v75) dst_sel:DWORD dst_unused:UNUSED_PAD src0_sel:BYTE_0
	v_cvt_f32_i32_sdwa v62, sext(v75) dst_sel:DWORD dst_unused:UNUSED_PAD src0_sel:BYTE_1
	v_cvt_f32_i32_sdwa v63, sext(v75) dst_sel:DWORD dst_unused:UNUSED_PAD src0_sel:BYTE_2
	v_cvt_f32_i32_sdwa v75, sext(v75) dst_sel:DWORD dst_unused:UNUSED_PAD src0_sel:BYTE_3
	v_fmaak_f32 v61, v60, v61, 0x4b400000
	v_fmaak_f32 v62, v60, v62, 0x4b400000
	v_fmaak_f32 v63, v60, v63, 0x4b400000
	v_fmaak_f32 v75, v60, v75, 0x4b400000
	v_perm_b32 v61, v62, v61, s17
	v_perm_b32 v75, v75, v63, s17
	v_lshl_or_b32 v75, v75, 16, v61
	v_cvt_f32_i32_sdwa v61, sext(v76) dst_sel:DWORD dst_unused:UNUSED_PAD src0_sel:BYTE_0
	v_cvt_f32_i32_sdwa v62, sext(v76) dst_sel:DWORD dst_unused:UNUSED_PAD src0_sel:BYTE_1
	v_cvt_f32_i32_sdwa v63, sext(v76) dst_sel:DWORD dst_unused:UNUSED_PAD src0_sel:BYTE_2
	v_cvt_f32_i32_sdwa v76, sext(v76) dst_sel:DWORD dst_unused:UNUSED_PAD src0_sel:BYTE_3
	v_fmaak_f32 v61, v60, v61, 0x4b400000
	v_fmaak_f32 v62, v60, v62, 0x4b400000
	v_fmaak_f32 v63, v60, v63, 0x4b400000
	v_fmaak_f32 v76, v60, v76, 0x4b400000
	v_perm_b32 v61, v62, v61, s17
	v_perm_b32 v76, v76, v63, s17
	v_lshl_or_b32 v76, v76, 16, v61
	v_cvt_f32_i32_sdwa v61, sext(v77) dst_sel:DWORD dst_unused:UNUSED_PAD src0_sel:BYTE_0
	v_cvt_f32_i32_sdwa v62, sext(v77) dst_sel:DWORD dst_unused:UNUSED_PAD src0_sel:BYTE_1
	v_cvt_f32_i32_sdwa v63, sext(v77) dst_sel:DWORD dst_unused:UNUSED_PAD src0_sel:BYTE_2
	v_cvt_f32_i32_sdwa v77, sext(v77) dst_sel:DWORD dst_unused:UNUSED_PAD src0_sel:BYTE_3
	v_fmaak_f32 v61, v60, v61, 0x4b400000
	v_fmaak_f32 v62, v60, v62, 0x4b400000
	v_fmaak_f32 v63, v60, v63, 0x4b400000
	v_fmaak_f32 v77, v60, v77, 0x4b400000
	v_perm_b32 v61, v62, v61, s17
	v_perm_b32 v77, v77, v63, s17
	v_lshl_or_b32 v77, v77, 16, v61
	v_cvt_f32_i32_sdwa v61, sext(v70) dst_sel:DWORD dst_unused:UNUSED_PAD src0_sel:BYTE_0
	v_cvt_f32_i32_sdwa v62, sext(v70) dst_sel:DWORD dst_unused:UNUSED_PAD src0_sel:BYTE_1
	v_cvt_f32_i32_sdwa v63, sext(v70) dst_sel:DWORD dst_unused:UNUSED_PAD src0_sel:BYTE_2
	v_cvt_f32_i32_sdwa v70, sext(v70) dst_sel:DWORD dst_unused:UNUSED_PAD src0_sel:BYTE_3
	v_fmaak_f32 v61, v60, v61, 0x4b400000
	v_fmaak_f32 v62, v60, v62, 0x4b400000
	v_fmaak_f32 v63, v60, v63, 0x4b400000
	v_fmaak_f32 v70, v60, v70, 0x4b400000
	v_perm_b32 v61, v62, v61, s17
	v_perm_b32 v70, v70, v63, s17
	v_lshl_or_b32 v70, v70, 16, v61
	v_cvt_f32_i32_sdwa v61, sext(v71) dst_sel:DWORD dst_unused:UNUSED_PAD src0_sel:BYTE_0
	v_cvt_f32_i32_sdwa v62, sext(v71) dst_sel:DWORD dst_unused:UNUSED_PAD src0_sel:BYTE_1
	v_cvt_f32_i32_sdwa v63, sext(v71) dst_sel:DWORD dst_unused:UNUSED_PAD src0_sel:BYTE_2
	v_cvt_f32_i32_sdwa v71, sext(v71) dst_sel:DWORD dst_unused:UNUSED_PAD src0_sel:BYTE_3
	v_fmaak_f32 v61, v60, v61, 0x4b400000
	v_fmaak_f32 v62, v60, v62, 0x4b400000
	v_fmaak_f32 v63, v60, v63, 0x4b400000
	v_fmaak_f32 v71, v60, v71, 0x4b400000
	v_perm_b32 v61, v62, v61, s17
	v_perm_b32 v71, v71, v63, s17
	v_lshl_or_b32 v71, v71, 16, v61
	v_cvt_f32_i32_sdwa v61, sext(v72) dst_sel:DWORD dst_unused:UNUSED_PAD src0_sel:BYTE_0
	v_cvt_f32_i32_sdwa v62, sext(v72) dst_sel:DWORD dst_unused:UNUSED_PAD src0_sel:BYTE_1
	v_cvt_f32_i32_sdwa v63, sext(v72) dst_sel:DWORD dst_unused:UNUSED_PAD src0_sel:BYTE_2
	v_cvt_f32_i32_sdwa v72, sext(v72) dst_sel:DWORD dst_unused:UNUSED_PAD src0_sel:BYTE_3
	v_fmaak_f32 v61, v60, v61, 0x4b400000
	v_fmaak_f32 v62, v60, v62, 0x4b400000
	v_fmaak_f32 v63, v60, v63, 0x4b400000
	v_fmaak_f32 v72, v60, v72, 0x4b400000
	v_perm_b32 v61, v62, v61, s17
	v_perm_b32 v72, v72, v63, s17
	v_lshl_or_b32 v72, v72, 16, v61
	v_cvt_f32_i32_sdwa v61, sext(v73) dst_sel:DWORD dst_unused:UNUSED_PAD src0_sel:BYTE_0
	v_cvt_f32_i32_sdwa v62, sext(v73) dst_sel:DWORD dst_unused:UNUSED_PAD src0_sel:BYTE_1
	v_cvt_f32_i32_sdwa v63, sext(v73) dst_sel:DWORD dst_unused:UNUSED_PAD src0_sel:BYTE_2
	v_cvt_f32_i32_sdwa v73, sext(v73) dst_sel:DWORD dst_unused:UNUSED_PAD src0_sel:BYTE_3
	v_fmaak_f32 v61, v60, v61, 0x4b400000
	v_fmaak_f32 v62, v60, v62, 0x4b400000
	v_fmaak_f32 v63, v60, v63, 0x4b400000
	v_fmaak_f32 v60, v60, v73, 0x4b400000
	v_perm_b32 v73, v62, v61, s17
	v_perm_b32 v60, v60, v63, s17
	v_lshl_or_b32 v73, v60, 16, v73
	global_store_dwordx4 v[80:81], v[74:77], off
	global_store_dwordx4 v[80:81], v[70:73], off offset:16
	s_and_saveexec_b64 s[6:7], s[0:1]
	s_cbranch_execz .Lq1293_B
	s_ashr_i32 s5, s4, 31
	s_lshl_b64 s[12:13], s[4:5], 2
	v_mul_f32_e32 v60, 0x3c010204, v23
	s_add_u32 s12, s10, s12
	v_cndmask_b32_e32 v60, 1.0, v60, vcc
	s_addc_u32 s13, s11, s13
	global_store_dword v11, v60, s[12:13]

.Lq1294_B:
	v_readlane_b32 s12, v252, 29
	s_add_i32 s6, s4, s12
	s_cmp_lt_i32 s6, s16
	v_readlane_b32 s13, v252, 30
	s_cbranch_scc0 .LBB0_1300
	s_branch .Lq_top_A
.LBB0_1300:
	s_waitcnt vmcnt(0)
	s_waitcnt lgkmcnt(0)
	s_barrier
	s_mov_b64 s[0:1], exec
	v_readlane_b32 s4, v252, 11
	v_readlane_b32 s5, v252, 12
	s_and_b64 s[4:5], s[0:1], s[4:5]
	s_mov_b64 exec, s[4:5]
	s_cbranch_execz .LBB0_1352
	s_add_i32 s4, 0, 0x26f20
	v_mov_b32_e32 v0, s4
	s_waitcnt vmcnt(0) expcnt(0) lgkmcnt(0)
	ds_read_b32 v3, v0
	s_add_i32 s4, 0, 0x26f24
	v_mov_b32_e32 v0, s4
	ds_read_b32 v1, v0
	s_waitcnt lgkmcnt(1)
	v_cmp_ne_u32_e32 vcc, 0, v3
	s_cbranch_vccnz .LBB0_1316
	v_readlane_b32 s4, v252, 4
	v_readlane_b32 s5, v252, 5
	s_load_dwordx2 s[12:13], s[4:5], 0x4
	v_readlane_b32 s42, v252, 2
	v_readlane_b32 s43, v252, 3
	s_add_u32 s4, s42, 0x4200
	s_addc_u32 s5, s43, 0
	s_add_u32 s6, s42, 0x4400
	s_addc_u32 s7, s43, 0
	v_readlane_b32 s14, v252, 6
	s_waitcnt lgkmcnt(0)
	s_mul_i32 s51, s12, s14
	s_add_u32 s12, s42, 0x4500
	s_mul_i32 s51, s51, s13
	s_addc_u32 s13, s43, 0
	v_readlane_b32 s15, v252, 7
	s_add_u32 s14, s42, 0x4600
	s_addc_u32 s15, s43, 0
	s_add_u32 s16, s42, 0x4700
	s_addc_u32 s17, s43, 0
	s_add_u32 s18, s42, 0x4800
	s_addc_u32 s19, s43, 0
	s_add_u32 s20, s42, 0x4900
	s_addc_u32 s21, s43, 0
	s_add_u32 s22, s42, 0x4a00
	s_addc_u32 s23, s43, 0
	s_add_u32 s24, s42, 0x4b00
	s_addc_u32 s25, s43, 0
	s_add_u32 s26, s42, 0x4c00
	s_addc_u32 s27, s43, 0
	s_add_u32 s28, s42, 0x4d00
	s_addc_u32 s29, s43, 0
	s_add_u32 s30, s42, 0x4e00
	s_addc_u32 s31, s43, 0
	s_add_u32 s34, s42, 0x4f00
	s_addc_u32 s35, s43, 0
	s_add_u32 s36, s42, 0x5000
	s_addc_u32 s37, s43, 0
	s_add_u32 s38, s42, 0x5100
	s_addc_u32 s39, s43, 0
	s_add_u32 s40, s42, 0x5200
	s_addc_u32 s41, s43, 0
	s_add_u32 s42, s42, 0x5300
	s_addc_u32 s43, s43, 0
	s_mov_b32 s52, 1
	v_mov_b32_e32 v17, 0
	s_branch .LBB0_1304
	s_nop 0
	s_nop 0
	s_nop 0
	s_nop 0
